# adds: RG-LRU pass-2 conv loads batched; hyena filter layer-2 weights preloaded once per column
# speedup vs baseline: 1.0018x; 1.0018x over previous
; __device__ __forceinline__ void lds_barrier() { asm volatile("s_waitcnt lgkmcnt(0)" ::: "memory"); __builtin_amdgcn_s_barrier(); asm volatile("" ::: "memory"); }
;     ...
;             lds_barrier();
;             for (int o = F.tid; o < 16 * 64; o += 512) { const int p = o >> 6, j = o & 63; float s = b2[j];
; #pragma unroll 8
;                 for (int i = 0; i < 64; ++i) s += f1[p * 64 + i] * w2[i * 64 + j];
;                 f2[o] = sinf(fq[j] * s); }
.LBB0_248:
	s_or_b64 exec, exec, s[0:1]
	s_waitcnt lgkmcnt(0)
	s_barrier
	s_and_saveexec_b64 s[0:1], s[42:43]
	s_cbranch_execz .LBB0_257
	global_load_dword v18, v[10:11], off
	global_load_dword v19, v[8:9], off
	s_mov_b64 s[6:7], 0x1000
	v_lshl_add_u64 v[188:189], v[14:15], 0, s[6:7]
	v_lshl_add_u64 v[190:191], v[188:189], 0, s[6:7]
	v_lshl_add_u64 v[192:193], v[190:191], 0, s[6:7]
	global_load_dword v120, v[14:15], off
	global_load_dword v121, v[14:15], off offset:256
	global_load_dword v122, v[14:15], off offset:512
	global_load_dword v123, v[14:15], off offset:768
	global_load_dword v124, v[14:15], off offset:1024
	global_load_dword v125, v[14:15], off offset:1280
	global_load_dword v126, v[14:15], off offset:1536
	global_load_dword v127, v[14:15], off offset:1792
	global_load_dword v128, v[14:15], off offset:2048
	global_load_dword v129, v[14:15], off offset:2304
	global_load_dword v130, v[14:15], off offset:2560
	global_load_dword v131, v[14:15], off offset:2816
	global_load_dword v132, v[14:15], off offset:3072
	global_load_dword v133, v[14:15], off offset:3328
	global_load_dword v134, v[14:15], off offset:3584
	global_load_dword v135, v[14:15], off offset:3840
	global_load_dword v136, v[188:189], off
	global_load_dword v137, v[188:189], off offset:256
	global_load_dword v138, v[188:189], off offset:512
	global_load_dword v139, v[188:189], off offset:768
	global_load_dword v140, v[188:189], off offset:1024
	global_load_dword v141, v[188:189], off offset:1280
	global_load_dword v142, v[188:189], off offset:1536
	global_load_dword v143, v[188:189], off offset:1792
	global_load_dword v144, v[188:189], off offset:2048
	global_load_dword v145, v[188:189], off offset:2304
	global_load_dword v146, v[188:189], off offset:2560
	global_load_dword v147, v[188:189], off offset:2816
	global_load_dword v148, v[188:189], off offset:3072
	global_load_dword v149, v[188:189], off offset:3328
	global_load_dword v150, v[188:189], off offset:3584
	global_load_dword v151, v[188:189], off offset:3840
	global_load_dword v152, v[190:191], off
	global_load_dword v153, v[190:191], off offset:256
	global_load_dword v154, v[190:191], off offset:512
	global_load_dword v155, v[190:191], off offset:768
	global_load_dword v156, v[190:191], off offset:1024
	global_load_dword v157, v[190:191], off offset:1280
	global_load_dword v158, v[190:191], off offset:1536
	global_load_dword v159, v[190:191], off offset:1792
	global_load_dword v160, v[190:191], off offset:2048
	global_load_dword v161, v[190:191], off offset:2304
	global_load_dword v162, v[190:191], off offset:2560
	global_load_dword v163, v[190:191], off offset:2816
	global_load_dword v164, v[190:191], off offset:3072
	global_load_dword v165, v[190:191], off offset:3328
	global_load_dword v166, v[190:191], off offset:3584
	global_load_dword v167, v[190:191], off offset:3840
	s_waitcnt vmcnt(32)
	global_load_dword v168, v[192:193], off
	global_load_dword v169, v[192:193], off offset:256
	global_load_dword v170, v[192:193], off offset:512
	global_load_dword v171, v[192:193], off offset:768
	global_load_dword v172, v[192:193], off offset:1024
	global_load_dword v173, v[192:193], off offset:1280
	global_load_dword v174, v[192:193], off offset:1536
	global_load_dword v175, v[192:193], off offset:1792
	global_load_dword v176, v[192:193], off offset:2048
	global_load_dword v177, v[192:193], off offset:2304
	global_load_dword v178, v[192:193], off offset:2560
	global_load_dword v179, v[192:193], off offset:2816
	global_load_dword v180, v[192:193], off offset:3072
	global_load_dword v182, v[192:193], off offset:3328
	global_load_dword v183, v[192:193], off offset:3584
	global_load_dword v186, v[192:193], off offset:3840
	s_mov_b64 s[2:3], 0
	v_mov_b32_e32 v20, v0
	s_branch .LBB0_251

;     ...
;             for (int o = F.tid; o < 16 * 64; o += 512) { const int p = o >> 6, j = o & 63; float s = b2[j];
; #pragma unroll 8
;                 for (int i = 0; i < 64; ++i) s += f1[p * 64 + i] * w2[i * 64 + j];
;                 f2[o] = sinf(fq[j] * s); }
.LBB0_251:
	v_lshlrev_b32_e32 v21, 2, v20
	v_and_b32_e32 v21, 0xffffff00, v21
	s_add_i32 s4, 0, 0x800
	v_add_u32_e32 v21, s4, v21
	s_mov_b64 s[4:5], 0
	s_waitcnt vmcnt(0)
	v_mov_b32_e32 v22, v18
	ds_read_b128 v[56:59], v21
	ds_read_b128 v[60:63], v21 offset:16
	ds_read_b128 v[64:67], v21 offset:32
	ds_read_b128 v[68:71], v21 offset:48
	ds_read_b128 v[72:75], v21 offset:64
	ds_read_b128 v[76:79], v21 offset:80
	ds_read_b128 v[80:83], v21 offset:96
	ds_read_b128 v[84:87], v21 offset:112
	s_waitcnt lgkmcnt(0)
	ds_read_b128 v[88:91], v21 offset:128
	ds_read_b128 v[92:95], v21 offset:144
	ds_read_b128 v[96:99], v21 offset:160
	ds_read_b128 v[100:103], v21 offset:176
	ds_read_b128 v[104:107], v21 offset:192
	ds_read_b128 v[108:111], v21 offset:208
	ds_read_b128 v[112:115], v21 offset:224
	ds_read_b128 v[116:119], v21 offset:240
	v_fmac_f32_e32 v22, v56, v120
	v_fmac_f32_e32 v22, v57, v121
	v_fmac_f32_e32 v22, v58, v122
	v_fmac_f32_e32 v22, v59, v123
	v_fmac_f32_e32 v22, v60, v124
	v_fmac_f32_e32 v22, v61, v125
	v_fmac_f32_e32 v22, v62, v126
	v_fmac_f32_e32 v22, v63, v127
	v_fmac_f32_e32 v22, v64, v128
	v_fmac_f32_e32 v22, v65, v129
	v_fmac_f32_e32 v22, v66, v130
	v_fmac_f32_e32 v22, v67, v131
	v_fmac_f32_e32 v22, v68, v132
	v_fmac_f32_e32 v22, v69, v133
	v_fmac_f32_e32 v22, v70, v134
	v_fmac_f32_e32 v22, v71, v135
	v_fmac_f32_e32 v22, v72, v136
	v_fmac_f32_e32 v22, v73, v137
	v_fmac_f32_e32 v22, v74, v138
	v_fmac_f32_e32 v22, v75, v139
	v_fmac_f32_e32 v22, v76, v140
	v_fmac_f32_e32 v22, v77, v141
	v_fmac_f32_e32 v22, v78, v142
	v_fmac_f32_e32 v22, v79, v143
	v_fmac_f32_e32 v22, v80, v144
	v_fmac_f32_e32 v22, v81, v145
	v_fmac_f32_e32 v22, v82, v146
	v_fmac_f32_e32 v22, v83, v147
	v_fmac_f32_e32 v22, v84, v148
	v_fmac_f32_e32 v22, v85, v149
	v_fmac_f32_e32 v22, v86, v150
	v_fmac_f32_e32 v22, v87, v151
	s_waitcnt lgkmcnt(0)
	v_fmac_f32_e32 v22, v88, v152
	v_fmac_f32_e32 v22, v89, v153
	v_fmac_f32_e32 v22, v90, v154
	v_fmac_f32_e32 v22, v91, v155
	v_fmac_f32_e32 v22, v92, v156
	v_fmac_f32_e32 v22, v93, v157
	v_fmac_f32_e32 v22, v94, v158
	v_fmac_f32_e32 v22, v95, v159
	v_fmac_f32_e32 v22, v96, v160
	v_fmac_f32_e32 v22, v97, v161
	v_fmac_f32_e32 v22, v98, v162
	v_fmac_f32_e32 v22, v99, v163
	v_fmac_f32_e32 v22, v100, v164
	v_fmac_f32_e32 v22, v101, v165
	v_fmac_f32_e32 v22, v102, v166
	v_fmac_f32_e32 v22, v103, v167
	v_fmac_f32_e32 v22, v104, v168
	v_fmac_f32_e32 v22, v105, v169
	v_fmac_f32_e32 v22, v106, v170
	v_fmac_f32_e32 v22, v107, v171
	v_fmac_f32_e32 v22, v108, v172
	v_fmac_f32_e32 v22, v109, v173
	v_fmac_f32_e32 v22, v110, v174
	v_fmac_f32_e32 v22, v111, v175
	v_fmac_f32_e32 v22, v112, v176
	v_fmac_f32_e32 v22, v113, v177
	v_fmac_f32_e32 v22, v114, v178
	v_fmac_f32_e32 v22, v115, v179
	v_fmac_f32_e32 v22, v116, v180
	v_fmac_f32_e32 v22, v117, v182
	v_fmac_f32_e32 v22, v118, v183
	v_fmac_f32_e32 v22, v119, v186
	v_mul_f32_e32 v21, v22, v19
	s_brev_b32 s4, 18
	v_and_b32_e32 v22, 0x7fffffff, v21
	v_cmp_nlt_f32_e64 s[4:5], |v21|, s4
	s_and_saveexec_b64 s[6:7], s[4:5]
	s_xor_b64 s[4:5], exec, s[6:7]
	s_cbranch_execz .LBB0_255
	v_lshrrev_b32_e32 v23, 23, v22
	v_add_u32_e32 v23, 0xffffff88, v23
	v_cmp_lt_u32_e32 vcc, 63, v23
	s_mov_b32 s6, 0xfe5163ab
	s_nop 0
	v_cndmask_b32_e32 v24, 0, v214, vcc
	v_add_u32_e32 v23, v24, v23
	v_cmp_lt_u32_e64 s[44:45], 31, v23
	s_nop 1
	v_cndmask_b32_e64 v24, 0, v201, s[44:45]
	v_add_u32_e32 v23, v24, v23
	v_cmp_lt_u32_e64 s[46:47], 31, v23
	s_nop 1
	v_cndmask_b32_e64 v24, 0, v201, s[46:47]
	v_add_u32_e32 v23, v24, v23
	v_and_b32_e32 v24, 0x7fffff, v22
	v_or_b32_e32 v36, 0x800000, v24
	v_mad_u64_u32 v[24:25], s[6:7], v36, s6, 0
	v_mov_b32_e32 v180, v25
	s_mov_b32 s6, 0x3c439041
	v_mad_u64_u32 v[26:27], s[6:7], v36, s6, v[180:181]
	v_mov_b32_e32 v180, v27
	s_mov_b32 s6, 0xdb629599
	v_mad_u64_u32 v[28:29], s[6:7], v36, s6, v[180:181]
	v_mov_b32_e32 v180, v29
	s_mov_b32 s6, 0xf534ddc0
	v_mad_u64_u32 v[30:31], s[6:7], v36, s6, v[180:181]
	v_mov_b32_e32 v180, v31
	s_mov_b32 s6, 0xfc2757d1
	v_mad_u64_u32 v[32:33], s[6:7], v36, s6, v[180:181]
	v_mov_b32_e32 v180, v33
	s_mov_b32 s6, 0x4e441529
	v_mad_u64_u32 v[34:35], s[6:7], v36, s6, v[180:181]
	v_mov_b32_e32 v180, v35
	s_mov_b32 s6, 0xa2f9836e
	v_mad_u64_u32 v[36:37], s[6:7], v36, s6, v[180:181]
	v_cndmask_b32_e32 v25, v34, v30, vcc
	v_cndmask_b32_e32 v27, v36, v32, vcc
	v_cndmask_b32_e32 v31, v37, v34, vcc
	v_cndmask_b32_e64 v29, v27, v25, s[44:45]
	v_cndmask_b32_e64 v27, v31, v27, s[44:45]
	v_cndmask_b32_e32 v31, v32, v28, vcc
	v_cndmask_b32_e64 v25, v25, v31, s[44:45]
	v_cndmask_b32_e64 v27, v27, v29, s[46:47]
	v_cndmask_b32_e64 v29, v29, v25, s[46:47]
	v_sub_u32_e32 v32, 32, v23
	v_alignbit_b32 v33, v27, v29, v32
	v_cmp_eq_u32_e64 s[50:51], 0, v23
	v_cndmask_b32_e32 v26, v30, v26, vcc
	v_cndmask_b32_e32 v24, v28, v24, vcc
	v_cndmask_b32_e64 v23, v33, v27, s[50:51]
	v_cndmask_b32_e64 v27, v31, v26, s[44:45]
	v_cndmask_b32_e64 v25, v25, v27, s[46:47]
	v_alignbit_b32 v30, v29, v25, v32
	v_cndmask_b32_e64 v29, v30, v29, s[50:51]
	v_bfe_u32 v33, v23, 29, 1
	v_cndmask_b32_e64 v24, v26, v24, s[44:45]
	v_alignbit_b32 v30, v23, v29, 30
	v_sub_u32_e32 v34, 0, v33
	v_cndmask_b32_e64 v24, v27, v24, s[46:47]
	v_xor_b32_e32 v30, v30, v34
	v_alignbit_b32 v26, v25, v24, v32
	v_cndmask_b32_e64 v25, v26, v25, s[50:51]
	v_ffbh_u32_e32 v27, v30
	v_alignbit_b32 v26, v29, v25, 30
	v_min_u32_e32 v27, 32, v27
	v_alignbit_b32 v24, v25, v24, 30
	v_xor_b32_e32 v26, v26, v34
	v_sub_u32_e32 v28, 31, v27
	v_xor_b32_e32 v24, v24, v34
	v_alignbit_b32 v29, v30, v26, v28
	v_alignbit_b32 v24, v26, v24, v28
	v_alignbit_b32 v25, v29, v24, 9
	v_ffbh_u32_e32 v26, v25
	v_min_u32_e32 v26, 32, v26
	v_lshrrev_b32_e32 v31, 29, v23
	v_not_b32_e32 v28, v26
	v_alignbit_b32 v24, v25, v24, v28
	v_lshlrev_b32_e32 v25, 31, v31
	v_or_b32_e32 v28, 0x33000000, v25
	v_add_lshl_u32 v26, v26, v27, 23
	v_lshrrev_b32_e32 v24, 9, v24
	v_sub_u32_e32 v26, v28, v26
	v_or_b32_e32 v25, 0.5, v25
	v_lshlrev_b32_e32 v27, 23, v27
	v_or_b32_e32 v24, v26, v24
	v_lshrrev_b32_e32 v26, 9, v29
	v_sub_u32_e32 v25, v25, v27
	v_or_b32_e32 v25, v26, v25
	v_mul_f32_e32 v26, 0x3fc90fda, v25
	s_mov_b32 s6, 0x3fc90fda
	v_fma_f32 v27, v25, s6, -v26
	v_fmac_f32_e32 v27, 0x33a22168, v25
	v_fmac_f32_e32 v27, 0x3fc90fda, v24
	v_lshrrev_b32_e32 v23, 30, v23
	v_add_f32_e32 v24, v26, v27
	v_add_u32_e32 v23, v33, v23

; #define LAS __attribute__((address_space(3)))
; __device__ __forceinline__ unsigned pk2(float lo, float hi) { const f32x2cv v = {lo, hi}; return __builtin_bit_cast(unsigned, __builtin_convertvector(v, bf16x2cv)); }
; __device__ __forceinline__ void lds_barrier() { asm volatile("s_waitcnt lgkmcnt(0)" ::: "memory"); __builtin_amdgcn_s_barrier(); asm volatile("" ::: "memory"); }
; template <int PASS>
; __device__ __forceinline__ void phase_rg(Frame& F0, const Args& A, int l) {
;     ...
;         int u = F.vcu + it * F.G, ng_lo = 0, ng_hi = 4;
;         if (F.G == 256 && it == 2) { if (F.vcu >= 128) { const int pc = F.vcu - 128; u = 512 + (pc >> 2); ng_lo = pc & 3; ng_hi = ng_lo + 1; } else u = ntile; }
;         if (u >= ntile) continue;
;         const int R0 = u * 64; const bool lat = R0 < ML; const int L = lat ? T : LC; const int t0 = lat ? (R0 & 4095) : ((R0 - ML) & 255);
;         lds_barrier(); tm_seg(F, 24);
;         { const int tok = F.tid >> 3, cg = (F.tid & 7) * 32; const int t = t0 + tok;
; #pragma unroll
;             for (int c8 = 0; c8 < 4; ++c8) { const int ch = cg + c8 * 8; float acc[8];
; #pragma unroll
;                 for (int j = 0; j < 8; ++j) acc[j] = CW[1024 + ch + j];
; #pragma unroll
;                 for (int tap = 0; tap < 4; ++tap) { const int tt = t - 1 + tap;
;                     if (tt >= 0 && tt < L) { const v4u w = *(const v4u*)(P + (size_t)(R0 + tok - 1 + tap) * PROJ + C_RGX + ch); const LAS float* cwp = CW + tap * 256 + ch;
;                         acc[0] += bflo(w.x) * cwp[0]; acc[1] += bfhi(w.x) * cwp[1]; acc[2] += bflo(w.y) * cwp[2]; acc[3] += bfhi(w.y) * cwp[3];
;                         acc[4] += bflo(w.z) * cwp[4]; acc[5] += bfhi(w.z) * cwp[5]; acc[6] += bflo(w.w) * cwp[6]; acc[7] += bfhi(w.w) * cwp[7]; } }
;                 v4u o; o.x = pk2(acc[0], acc[1]); o.y = pk2(acc[2], acc[3]); o.z = pk2(acc[4], acc[5]); o.w = pk2(acc[6], acc[7]);
;                 *(LAS v4u*)(UB + tok * 264 + ch) = o; } }
.LBB0_657:
	s_mul_i32 s0, s8, s70
	v_readlane_b32 s1, v254, 12
	s_add_i32 s2, s0, s1
	s_cmp_lg_u32 s8, 2
	v_readlane_b32 s4, v253, 1
	s_cselect_b64 s[0:1], -1, 0
	v_readlane_b32 s5, v253, 2
	s_or_b64 s[20:21], s[4:5], s[0:1]
	s_and_b64 s[0:1], s[20:21], exec
	s_cselect_b32 s2, s2, s7
	s_cmp_ge_i32 s2, s26
	s_cbranch_scc1 .LBB0_656
	s_lshl_b32 s9, s2, 6
	s_cmpk_gt_i32 s2, 0x1ff
	s_cselect_b64 s[24:25], -1, 0
	s_cmpk_lt_i32 s2, 0x200
	s_cselect_b64 s[22:23], -1, 0
	s_and_b64 s[0:1], s[22:23], exec
	s_waitcnt lgkmcnt(0)
	s_barrier
	s_movk_i32 s0, 0xfc0
	s_waitcnt vmcnt(0)
	s_cselect_b32 s0, s0, 0xc0
	s_cselect_b32 s3, s48, 0x100
	s_and_b32 s4, s0, s9
	v_add_u32_e32 v12, s4, v147
	v_add_u32_e32 v8, s9, v147
	v_cmp_gt_u32_e64 s[38:39], s3, v12
	v_add_u32_e32 v10, 1, v12
	v_cmp_gt_u32_e64 s[40:41], s3, v10
	v_add_u32_e32 v10, 2, v12
	v_cmp_gt_u32_e64 s[42:43], s3, v10
	v_add_u32_e32 v10, 3, v12
	v_cmp_gt_u32_e64 s[44:45], s3, v10
	v_ashrrev_i32_e32 v9, 31, v8
	v_lshlrev_b64 v[10:11], 12, v[8:9]
	v_lshl_add_u64 v[10:11], v[64:65], 0, v[10:11]
	s_mov_b64 s[14:15], 0x1000
	v_lshl_add_u64 v[12:13], v[10:11], 0, s[14:15]
	v_lshl_add_u64 v[14:15], v[12:13], 0, s[14:15]
	v_lshl_add_u64 v[50:51], v[14:15], 0, s[14:15]
	s_mov_b64 s[0:1], exec
	s_and_b64 exec, s[0:1], s[38:39]
	global_load_dwordx4 v[70:73], v[10:11], off offset:3072
	s_and_b64 exec, s[0:1], s[40:41]
	global_load_dwordx4 v[74:77], v[12:13], off offset:3072
	s_and_b64 exec, s[0:1], s[42:43]
	global_load_dwordx4 v[78:81], v[14:15], off offset:3072
	s_and_b64 exec, s[0:1], s[44:45]
	global_load_dwordx4 v[82:85], v[50:51], off offset:3072
	s_and_b64 exec, s[0:1], s[38:39]
	global_load_dwordx4 v[86:89], v[10:11], off offset:3088
	s_and_b64 exec, s[0:1], s[40:41]
	global_load_dwordx4 v[90:93], v[12:13], off offset:3088
	s_and_b64 exec, s[0:1], s[42:43]
	global_load_dwordx4 v[94:97], v[14:15], off offset:3088
	s_and_b64 exec, s[0:1], s[44:45]
	global_load_dwordx4 v[98:101], v[50:51], off offset:3088
	s_and_b64 exec, s[0:1], s[38:39]
	global_load_dwordx4 v[102:105], v[10:11], off offset:3104
	s_and_b64 exec, s[0:1], s[40:41]
	global_load_dwordx4 v[106:109], v[12:13], off offset:3104
	s_and_b64 exec, s[0:1], s[42:43]
	global_load_dwordx4 v[110:113], v[14:15], off offset:3104
	s_and_b64 exec, s[0:1], s[44:45]
	global_load_dwordx4 v[114:117], v[50:51], off offset:3104
	s_and_b64 exec, s[0:1], s[38:39]
	global_load_dwordx4 v[118:121], v[10:11], off offset:3120
	s_and_b64 exec, s[0:1], s[40:41]
	global_load_dwordx4 v[122:125], v[12:13], off offset:3120
	s_and_b64 exec, s[0:1], s[42:43]
	global_load_dwordx4 v[126:129], v[14:15], off offset:3120
	s_and_b64 exec, s[0:1], s[44:45]
	global_load_dwordx4 v[130:133], v[50:51], off offset:3120
	s_mov_b64 exec, s[0:1]
	ds_read_b128 v[4:7], v157 offset:4096
	ds_read_b128 v[0:3], v157 offset:4112
	ds_read_b128 v[16:19], v157
	ds_read_b128 v[20:23], v157 offset:16
	ds_read_b128 v[24:27], v157 offset:1024
	ds_read_b128 v[28:31], v157 offset:1040
	ds_read_b128 v[32:35], v157 offset:2048
	ds_read_b128 v[36:39], v157 offset:2064
	ds_read_b128 v[40:43], v157 offset:3072
	ds_read_b128 v[44:47], v157 offset:3088
	s_waitcnt vmcnt(12)
	s_waitcnt lgkmcnt(0)
	s_and_b64 exec, s[0:1], s[38:39]
	v_lshlrev_b32_e32 v48, 16, v70
	v_and_b32_e32 v49, 0xffff0000, v70
	v_pk_fma_f32 v[4:5], v[16:17], v[48:49], v[4:5]
	v_lshlrev_b32_e32 v48, 16, v71
	v_and_b32_e32 v49, 0xffff0000, v71
	v_pk_fma_f32 v[6:7], v[18:19], v[48:49], v[6:7]
	v_lshlrev_b32_e32 v48, 16, v72
	v_and_b32_e32 v49, 0xffff0000, v72
	v_pk_fma_f32 v[0:1], v[20:21], v[48:49], v[0:1]
	v_lshlrev_b32_e32 v48, 16, v73
	v_and_b32_e32 v49, 0xffff0000, v73
	v_pk_fma_f32 v[2:3], v[22:23], v[48:49], v[2:3]
	s_and_b64 exec, s[0:1], s[40:41]
	v_lshlrev_b32_e32 v48, 16, v74
	v_and_b32_e32 v49, 0xffff0000, v74
	v_pk_fma_f32 v[4:5], v[24:25], v[48:49], v[4:5]
	v_lshlrev_b32_e32 v48, 16, v75
	v_and_b32_e32 v49, 0xffff0000, v75
	v_pk_fma_f32 v[6:7], v[26:27], v[48:49], v[6:7]
	v_lshlrev_b32_e32 v48, 16, v76
	v_and_b32_e32 v49, 0xffff0000, v76
	v_pk_fma_f32 v[0:1], v[28:29], v[48:49], v[0:1]
	v_lshlrev_b32_e32 v48, 16, v77
	v_and_b32_e32 v49, 0xffff0000, v77
	v_pk_fma_f32 v[2:3], v[30:31], v[48:49], v[2:3]
	s_and_b64 exec, s[0:1], s[42:43]
	v_lshlrev_b32_e32 v48, 16, v78
	v_and_b32_e32 v49, 0xffff0000, v78
	v_pk_fma_f32 v[4:5], v[32:33], v[48:49], v[4:5]
	v_lshlrev_b32_e32 v48, 16, v79
	v_and_b32_e32 v49, 0xffff0000, v79
	v_pk_fma_f32 v[6:7], v[34:35], v[48:49], v[6:7]
	v_lshlrev_b32_e32 v48, 16, v80
	v_and_b32_e32 v49, 0xffff0000, v80
	v_pk_fma_f32 v[0:1], v[36:37], v[48:49], v[0:1]
	v_lshlrev_b32_e32 v48, 16, v81
	v_and_b32_e32 v49, 0xffff0000, v81
	v_pk_fma_f32 v[2:3], v[38:39], v[48:49], v[2:3]
	s_and_b64 exec, s[0:1], s[44:45]
	v_lshlrev_b32_e32 v48, 16, v82
	v_and_b32_e32 v49, 0xffff0000, v82
	v_pk_fma_f32 v[4:5], v[40:41], v[48:49], v[4:5]
	v_lshlrev_b32_e32 v48, 16, v83
	v_and_b32_e32 v49, 0xffff0000, v83
	v_pk_fma_f32 v[6:7], v[42:43], v[48:49], v[6:7]
	v_lshlrev_b32_e32 v48, 16, v84
	v_and_b32_e32 v49, 0xffff0000, v84
	v_pk_fma_f32 v[0:1], v[44:45], v[48:49], v[0:1]
	v_lshlrev_b32_e32 v48, 16, v85
	v_and_b32_e32 v49, 0xffff0000, v85
	v_pk_fma_f32 v[2:3], v[46:47], v[48:49], v[2:3]
	s_mov_b64 exec, s[0:1]
	v_cvt_pk_bf16_f32 v4, v4, v5
	v_cvt_pk_bf16_f32 v5, v6, v7
	v_cvt_pk_bf16_f32 v6, v0, v1
	v_cvt_pk_bf16_f32 v7, v2, v3
	ds_write_b128 v158, v[4:7]
	s_mov_b64 exec, s[0:1]
	ds_read_b128 v[4:7], v159 offset:4096
	ds_read_b128 v[0:3], v159 offset:4112
	ds_read_b128 v[16:19], v159
	ds_read_b128 v[20:23], v159 offset:16
	ds_read_b128 v[24:27], v159 offset:1024
	ds_read_b128 v[28:31], v159 offset:1040
	ds_read_b128 v[32:35], v159 offset:2048
	ds_read_b128 v[36:39], v159 offset:2064
	ds_read_b128 v[40:43], v159 offset:3072
	ds_read_b128 v[44:47], v159 offset:3088
	s_waitcnt vmcnt(8)
; #define LAS __attribute__((address_space(3)))
; __device__ __forceinline__ unsigned pk2(float lo, float hi) { const f32x2cv v = {lo, hi}; return __builtin_bit_cast(unsigned, __builtin_convertvector(v, bf16x2cv)); }
; template <int PASS>
; __device__ __forceinline__ void phase_rg(Frame& F0, const Args& A, int l) {
;     ...
;         { const int tok = F.tid >> 3, cg = (F.tid & 7) * 32; const int t = t0 + tok;
; #pragma unroll
;             for (int c8 = 0; c8 < 4; ++c8) { const int ch = cg + c8 * 8; float acc[8];
; #pragma unroll
;                 for (int j = 0; j < 8; ++j) acc[j] = CW[1024 + ch + j];
; #pragma unroll
;                 for (int tap = 0; tap < 4; ++tap) { const int tt = t - 1 + tap;
;                     if (tt >= 0 && tt < L) { const v4u w = *(const v4u*)(P + (size_t)(R0 + tok - 1 + tap) * PROJ + C_RGX + ch); const LAS float* cwp = CW + tap * 256 + ch;
;                         acc[0] += bflo(w.x) * cwp[0]; acc[1] += bfhi(w.x) * cwp[1]; acc[2] += bflo(w.y) * cwp[2]; acc[3] += bfhi(w.y) * cwp[3];
;                         acc[4] += bflo(w.z) * cwp[4]; acc[5] += bfhi(w.z) * cwp[5]; acc[6] += bflo(w.w) * cwp[6]; acc[7] += bfhi(w.w) * cwp[7]; } }
;                 v4u o; o.x = pk2(acc[0], acc[1]); o.y = pk2(acc[2], acc[3]); o.z = pk2(acc[4], acc[5]); o.w = pk2(acc[6], acc[7]);
;                 *(LAS v4u*)(UB + tok * 264 + ch) = o; } }
	s_waitcnt lgkmcnt(0)
	s_and_b64 exec, s[0:1], s[38:39]
	v_lshlrev_b32_e32 v48, 16, v86
	v_and_b32_e32 v49, 0xffff0000, v86
	v_pk_fma_f32 v[4:5], v[16:17], v[48:49], v[4:5]
	v_lshlrev_b32_e32 v48, 16, v87
	v_and_b32_e32 v49, 0xffff0000, v87
	v_pk_fma_f32 v[6:7], v[18:19], v[48:49], v[6:7]
	v_lshlrev_b32_e32 v48, 16, v88
	v_and_b32_e32 v49, 0xffff0000, v88
	v_pk_fma_f32 v[0:1], v[20:21], v[48:49], v[0:1]
	v_lshlrev_b32_e32 v48, 16, v89
	v_and_b32_e32 v49, 0xffff0000, v89
	v_pk_fma_f32 v[2:3], v[22:23], v[48:49], v[2:3]
	s_and_b64 exec, s[0:1], s[40:41]
	v_lshlrev_b32_e32 v48, 16, v90
	v_and_b32_e32 v49, 0xffff0000, v90
	v_pk_fma_f32 v[4:5], v[24:25], v[48:49], v[4:5]
	v_lshlrev_b32_e32 v48, 16, v91
	v_and_b32_e32 v49, 0xffff0000, v91
	v_pk_fma_f32 v[6:7], v[26:27], v[48:49], v[6:7]
	v_lshlrev_b32_e32 v48, 16, v92
	v_and_b32_e32 v49, 0xffff0000, v92
	v_pk_fma_f32 v[0:1], v[28:29], v[48:49], v[0:1]
	v_lshlrev_b32_e32 v48, 16, v93
	v_and_b32_e32 v49, 0xffff0000, v93
	v_pk_fma_f32 v[2:3], v[30:31], v[48:49], v[2:3]
	s_and_b64 exec, s[0:1], s[42:43]
	v_lshlrev_b32_e32 v48, 16, v94
	v_and_b32_e32 v49, 0xffff0000, v94
	v_pk_fma_f32 v[4:5], v[32:33], v[48:49], v[4:5]
	v_lshlrev_b32_e32 v48, 16, v95
	v_and_b32_e32 v49, 0xffff0000, v95
	v_pk_fma_f32 v[6:7], v[34:35], v[48:49], v[6:7]
	v_lshlrev_b32_e32 v48, 16, v96
	v_and_b32_e32 v49, 0xffff0000, v96
	v_pk_fma_f32 v[0:1], v[36:37], v[48:49], v[0:1]
	v_lshlrev_b32_e32 v48, 16, v97
	v_and_b32_e32 v49, 0xffff0000, v97
	v_pk_fma_f32 v[2:3], v[38:39], v[48:49], v[2:3]
	s_and_b64 exec, s[0:1], s[44:45]
	v_lshlrev_b32_e32 v48, 16, v98
	v_and_b32_e32 v49, 0xffff0000, v98
	v_pk_fma_f32 v[4:5], v[40:41], v[48:49], v[4:5]
	v_lshlrev_b32_e32 v48, 16, v99
	v_and_b32_e32 v49, 0xffff0000, v99
	v_pk_fma_f32 v[6:7], v[42:43], v[48:49], v[6:7]
	v_lshlrev_b32_e32 v48, 16, v100
	v_and_b32_e32 v49, 0xffff0000, v100
	v_pk_fma_f32 v[0:1], v[44:45], v[48:49], v[0:1]
	v_lshlrev_b32_e32 v48, 16, v101
	v_and_b32_e32 v49, 0xffff0000, v101
	v_pk_fma_f32 v[2:3], v[46:47], v[48:49], v[2:3]
	s_mov_b64 exec, s[0:1]
	v_cvt_pk_bf16_f32 v4, v4, v5
	v_cvt_pk_bf16_f32 v5, v6, v7
	v_cvt_pk_bf16_f32 v6, v0, v1
	v_cvt_pk_bf16_f32 v7, v2, v3
	ds_write_b128 v158, v[4:7] offset:16
	s_mov_b64 exec, s[0:1]
	ds_read_b128 v[4:7], v160 offset:4096
	ds_read_b128 v[0:3], v160 offset:4112
	ds_read_b128 v[16:19], v160
	ds_read_b128 v[20:23], v160 offset:16
	ds_read_b128 v[24:27], v160 offset:1024
	ds_read_b128 v[28:31], v160 offset:1040
	ds_read_b128 v[32:35], v160 offset:2048
	ds_read_b128 v[36:39], v160 offset:2064
	ds_read_b128 v[40:43], v160 offset:3072
	ds_read_b128 v[44:47], v160 offset:3088
	s_waitcnt vmcnt(4)
	s_waitcnt lgkmcnt(0)
; #define LAS __attribute__((address_space(3)))
; __device__ __forceinline__ unsigned pk2(float lo, float hi) { const f32x2cv v = {lo, hi}; return __builtin_bit_cast(unsigned, __builtin_convertvector(v, bf16x2cv)); }
; template <int PASS>
; __device__ __forceinline__ void phase_rg(Frame& F0, const Args& A, int l) {
;     ...
;         { const int tok = F.tid >> 3, cg = (F.tid & 7) * 32; const int t = t0 + tok;
; #pragma unroll
;             for (int c8 = 0; c8 < 4; ++c8) { const int ch = cg + c8 * 8; float acc[8];
; #pragma unroll
;                 for (int j = 0; j < 8; ++j) acc[j] = CW[1024 + ch + j];
; #pragma unroll
;                 for (int tap = 0; tap < 4; ++tap) { const int tt = t - 1 + tap;
;                     if (tt >= 0 && tt < L) { const v4u w = *(const v4u*)(P + (size_t)(R0 + tok - 1 + tap) * PROJ + C_RGX + ch); const LAS float* cwp = CW + tap * 256 + ch;
;                         acc[0] += bflo(w.x) * cwp[0]; acc[1] += bfhi(w.x) * cwp[1]; acc[2] += bflo(w.y) * cwp[2]; acc[3] += bfhi(w.y) * cwp[3];
;                         acc[4] += bflo(w.z) * cwp[4]; acc[5] += bfhi(w.z) * cwp[5]; acc[6] += bflo(w.w) * cwp[6]; acc[7] += bfhi(w.w) * cwp[7]; } }
;                 v4u o; o.x = pk2(acc[0], acc[1]); o.y = pk2(acc[2], acc[3]); o.z = pk2(acc[4], acc[5]); o.w = pk2(acc[6], acc[7]);
;                 *(LAS v4u*)(UB + tok * 264 + ch) = o; } }
	s_and_b64 exec, s[0:1], s[38:39]
	v_lshlrev_b32_e32 v48, 16, v102
	v_and_b32_e32 v49, 0xffff0000, v102
	v_pk_fma_f32 v[4:5], v[16:17], v[48:49], v[4:5]
	v_lshlrev_b32_e32 v48, 16, v103
	v_and_b32_e32 v49, 0xffff0000, v103
	v_pk_fma_f32 v[6:7], v[18:19], v[48:49], v[6:7]
	v_lshlrev_b32_e32 v48, 16, v104
	v_and_b32_e32 v49, 0xffff0000, v104
	v_pk_fma_f32 v[0:1], v[20:21], v[48:49], v[0:1]
	v_lshlrev_b32_e32 v48, 16, v105
	v_and_b32_e32 v49, 0xffff0000, v105
	v_pk_fma_f32 v[2:3], v[22:23], v[48:49], v[2:3]
	s_and_b64 exec, s[0:1], s[40:41]
	v_lshlrev_b32_e32 v48, 16, v106
	v_and_b32_e32 v49, 0xffff0000, v106
	v_pk_fma_f32 v[4:5], v[24:25], v[48:49], v[4:5]
	v_lshlrev_b32_e32 v48, 16, v107
	v_and_b32_e32 v49, 0xffff0000, v107
	v_pk_fma_f32 v[6:7], v[26:27], v[48:49], v[6:7]
	v_lshlrev_b32_e32 v48, 16, v108
	v_and_b32_e32 v49, 0xffff0000, v108
	v_pk_fma_f32 v[0:1], v[28:29], v[48:49], v[0:1]
	v_lshlrev_b32_e32 v48, 16, v109
	v_and_b32_e32 v49, 0xffff0000, v109
	v_pk_fma_f32 v[2:3], v[30:31], v[48:49], v[2:3]
	s_and_b64 exec, s[0:1], s[42:43]
	v_lshlrev_b32_e32 v48, 16, v110
	v_and_b32_e32 v49, 0xffff0000, v110
	v_pk_fma_f32 v[4:5], v[32:33], v[48:49], v[4:5]
	v_lshlrev_b32_e32 v48, 16, v111
	v_and_b32_e32 v49, 0xffff0000, v111
	v_pk_fma_f32 v[6:7], v[34:35], v[48:49], v[6:7]
	v_lshlrev_b32_e32 v48, 16, v112
	v_and_b32_e32 v49, 0xffff0000, v112
	v_pk_fma_f32 v[0:1], v[36:37], v[48:49], v[0:1]
	v_lshlrev_b32_e32 v48, 16, v113
	v_and_b32_e32 v49, 0xffff0000, v113
	v_pk_fma_f32 v[2:3], v[38:39], v[48:49], v[2:3]
	s_and_b64 exec, s[0:1], s[44:45]
	v_lshlrev_b32_e32 v48, 16, v114
	v_and_b32_e32 v49, 0xffff0000, v114
	v_pk_fma_f32 v[4:5], v[40:41], v[48:49], v[4:5]
	v_lshlrev_b32_e32 v48, 16, v115
	v_and_b32_e32 v49, 0xffff0000, v115
	v_pk_fma_f32 v[6:7], v[42:43], v[48:49], v[6:7]
	v_lshlrev_b32_e32 v48, 16, v116
	v_and_b32_e32 v49, 0xffff0000, v116
	v_pk_fma_f32 v[0:1], v[44:45], v[48:49], v[0:1]
	v_lshlrev_b32_e32 v48, 16, v117
	v_and_b32_e32 v49, 0xffff0000, v117
	v_pk_fma_f32 v[2:3], v[46:47], v[48:49], v[2:3]
	s_mov_b64 exec, s[0:1]
	v_cvt_pk_bf16_f32 v4, v4, v5
	v_cvt_pk_bf16_f32 v5, v6, v7
	v_cvt_pk_bf16_f32 v6, v0, v1
	v_cvt_pk_bf16_f32 v7, v2, v3
	ds_write_b128 v158, v[4:7] offset:32
	s_mov_b64 exec, s[0:1]
	ds_read_b128 v[4:7], v161 offset:4096
	ds_read_b128 v[0:3], v161 offset:4112
	ds_read_b128 v[16:19], v161
	ds_read_b128 v[20:23], v161 offset:16
	ds_read_b128 v[24:27], v161 offset:1024
	ds_read_b128 v[28:31], v161 offset:1040
	ds_read_b128 v[32:35], v161 offset:2048
	ds_read_b128 v[36:39], v161 offset:2064
	ds_read_b128 v[40:43], v161 offset:3072
	ds_read_b128 v[44:47], v161 offset:3088
	s_waitcnt vmcnt(0)
	s_waitcnt lgkmcnt(0)
	s_and_b64 exec, s[0:1], s[38:39]
	v_lshlrev_b32_e32 v48, 16, v118
	v_and_b32_e32 v49, 0xffff0000, v118
	v_pk_fma_f32 v[4:5], v[16:17], v[48:49], v[4:5]
	v_lshlrev_b32_e32 v48, 16, v119
	v_and_b32_e32 v49, 0xffff0000, v119
	v_pk_fma_f32 v[6:7], v[18:19], v[48:49], v[6:7]
	v_lshlrev_b32_e32 v48, 16, v120
	v_and_b32_e32 v49, 0xffff0000, v120
	v_pk_fma_f32 v[0:1], v[20:21], v[48:49], v[0:1]
	v_lshlrev_b32_e32 v48, 16, v121
	v_and_b32_e32 v49, 0xffff0000, v121
	v_pk_fma_f32 v[2:3], v[22:23], v[48:49], v[2:3]
	s_and_b64 exec, s[0:1], s[40:41]
	v_lshlrev_b32_e32 v48, 16, v122
	v_and_b32_e32 v49, 0xffff0000, v122
	v_pk_fma_f32 v[4:5], v[24:25], v[48:49], v[4:5]
	v_lshlrev_b32_e32 v48, 16, v123
	v_and_b32_e32 v49, 0xffff0000, v123
	v_pk_fma_f32 v[6:7], v[26:27], v[48:49], v[6:7]
	v_lshlrev_b32_e32 v48, 16, v124
	v_and_b32_e32 v49, 0xffff0000, v124
	v_pk_fma_f32 v[0:1], v[28:29], v[48:49], v[0:1]
	v_lshlrev_b32_e32 v48, 16, v125
	v_and_b32_e32 v49, 0xffff0000, v125
	v_pk_fma_f32 v[2:3], v[30:31], v[48:49], v[2:3]
	s_and_b64 exec, s[0:1], s[42:43]
	v_lshlrev_b32_e32 v48, 16, v126
	v_and_b32_e32 v49, 0xffff0000, v126
	v_pk_fma_f32 v[4:5], v[32:33], v[48:49], v[4:5]
	v_lshlrev_b32_e32 v48, 16, v127
	v_and_b32_e32 v49, 0xffff0000, v127
	v_pk_fma_f32 v[6:7], v[34:35], v[48:49], v[6:7]
	v_lshlrev_b32_e32 v48, 16, v128
	v_and_b32_e32 v49, 0xffff0000, v128
	v_pk_fma_f32 v[0:1], v[36:37], v[48:49], v[0:1]
	v_lshlrev_b32_e32 v48, 16, v129
	v_and_b32_e32 v49, 0xffff0000, v129
	v_pk_fma_f32 v[2:3], v[38:39], v[48:49], v[2:3]
	s_and_b64 exec, s[0:1], s[44:45]
	v_lshlrev_b32_e32 v48, 16, v130
	v_and_b32_e32 v49, 0xffff0000, v130
	v_pk_fma_f32 v[4:5], v[40:41], v[48:49], v[4:5]
	v_lshlrev_b32_e32 v48, 16, v131
	v_and_b32_e32 v49, 0xffff0000, v131
	v_pk_fma_f32 v[6:7], v[42:43], v[48:49], v[6:7]
	v_lshlrev_b32_e32 v48, 16, v132
	v_and_b32_e32 v49, 0xffff0000, v132
	v_pk_fma_f32 v[0:1], v[44:45], v[48:49], v[0:1]
	v_lshlrev_b32_e32 v48, 16, v133
	v_and_b32_e32 v49, 0xffff0000, v133
	v_pk_fma_f32 v[2:3], v[46:47], v[48:49], v[2:3]

; template <int PASS>
; __device__ __forceinline__ void phase_rg(Frame& F0, const Args& A, int l) {
;     ...
;             const int dir = F.tid >> 8, ch = F.tid & 255; const int b = lat ? (u >> 6) : ((u - 512) >> 2); const int i = lat ? (u & 63) : ((u - 512) & 3);
;             const int pos = lat ? (dir ? 4 + 63 - i : 4 + i) : (dir ? 3 - i : i);
;             float h = 0.f;
;             for (int p0 = 0; p0 < pos; p0 += 17) { f32x2v cv[17];
.LBB0_683:
	s_waitcnt vmcnt(0)
	v_cmp_ne_u32_e32 vcc, 0, v36
	v_mov_b32_e32 v1, 0
	s_and_saveexec_b64 s[14:15], vcc
	s_cbranch_execnz .LBB0_695
	s_branch .LBB0_764
.LBB0_693:
	s_and_b32 s0, s2, 3
	s_xor_b32 s1, s0, 3
	v_mov_b32_e32 v0, s1
	v_mov_b32_e32 v1, s0
	s_waitcnt vmcnt(0)
	v_cndmask_b32_e64 v36, v0, v1, s[36:37]
	s_cbranch_execnz .LBB0_683
